# P3 and P13: removed the compiler-inserted vmcnt(0) in front of the V-tile ds_read_tr reads (it drained the next tiles' LDS-DMA prefetch); stacked on v015
# baseline (speedup 1.0000x reference)
.LBB0_269:
	v_pk_add_f32 v[114:115], v[98:99], 0 op_sel_hi:[1,0]
	v_max_i32_e32 v116, 0, v82
	v_pk_add_f32 v[114:115], v[100:101], v[114:115]
	v_max_i32_e32 v117, 0, v83
	v_pk_add_f32 v[114:115], v[102:103], v[114:115]
	v_max_i32_e32 v118, 0, v84
	v_pk_add_f32 v[114:115], v[104:105], v[114:115]
	v_max_i32_e32 v119, 0, v85
	v_pk_add_f32 v[114:115], v[106:107], v[114:115]
	v_max_i32_e32 v120, 0, v86
	v_pk_add_f32 v[114:115], v[108:109], v[114:115]
	v_max_i32_e32 v121, 0, v87
	v_pk_add_f32 v[114:115], v[110:111], v[114:115]
	v_max_i32_e32 v122, 0, v88
	v_pk_add_f32 v[114:115], v[112:113], v[114:115]
	v_max_i32_e32 v123, 0, v89
	v_pk_add_f32 v[204:205], v[114:115], v[114:115] op_sel:[0,1] op_sel_hi:[1,0]
	v_exp_f32_e64 v114, -|v82|
	v_exp_f32_e64 v115, -|v83|
	v_max_i32_e32 v124, 0, v90
	v_max_i32_e32 v125, 0, v91
	v_max_i32_e32 v126, 0, v92
	v_pk_add_f32 v[114:115], v[114:115], 1.0 op_sel_hi:[1,0]
	v_max_i32_e32 v127, 0, v93
	v_log_f32_e32 v114, v114
	v_log_f32_e32 v115, v115
	v_max_i32_e32 v128, 0, v94
	v_max_i32_e32 v129, 0, v95
	v_max_i32_e32 v208, 0, v96
	v_pk_add_f32 v[114:115], v[114:115], v[116:117]
	v_exp_f32_e64 v116, -|v84|
	v_exp_f32_e64 v117, -|v85|
	v_max_i32_e32 v209, 0, v97
	v_sub_f32_e32 v225, v203, v115
	v_sub_f32_e32 v224, v203, v114
	v_pk_add_f32 v[116:117], v[116:117], 1.0 op_sel_hi:[1,0]
	v_cvt_pk_bf16_f32 v98, v98, v99
	v_log_f32_e32 v116, v116
	v_log_f32_e32 v117, v117
	v_cvt_pk_bf16_f32 v99, v100, v101
	v_cvt_pk_bf16_f32 v100, v102, v103
	v_cvt_pk_bf16_f32 v101, v104, v105
	v_pk_add_f32 v[116:117], v[116:117], v[118:119]
	v_exp_f32_e64 v118, -|v86|
	v_exp_f32_e64 v119, -|v87|
	v_sub_f32_e32 v227, v203, v117
	v_sub_f32_e32 v226, v203, v116
	v_pk_add_f32 v[84:85], v[84:85], v[226:227]
	v_pk_add_f32 v[118:119], v[118:119], 1.0 op_sel_hi:[1,0]
	v_pk_add_f32 v[82:83], v[82:83], v[224:225]
	v_log_f32_e32 v118, v118
	v_log_f32_e32 v119, v119
	v_mfma_f32_32x32x16_bf16 v[66:81], v[130:133], v[98:101], v[66:81]
	v_cvt_pk_bf16_f32 v98, v114, v115
	v_cvt_pk_bf16_f32 v99, v116, v117
	v_add_f32_e64 v118, v118, v120
	v_add_f32_e64 v119, v119, v121
	v_exp_f32_e64 v120, -|v88|
	v_exp_f32_e64 v121, -|v89|
	v_sub_f32_e32 v229, v203, v119
	v_sub_f32_e32 v228, v203, v118
	v_pk_add_f32 v[86:87], v[86:87], v[228:229]
	v_pk_add_f32 v[120:121], v[120:121], 1.0 op_sel_hi:[1,0]
	v_cvt_pk_bf16_f32 v100, v118, v119
	v_log_f32_e32 v120, v120
	v_log_f32_e32 v121, v121
	v_add_u32_e32 v244, s81, v210
	v_mov_b32_e32 v206, v204
	s_nop 1
	v_permlane32_swap_b32_e32 v204, v206
	v_pk_add_f32 v[122:123], v[120:121], v[122:123]
	v_exp_f32_e64 v120, -|v90|
	v_exp_f32_e64 v121, -|v91|
	v_sub_f32_e32 v231, v203, v123
	v_sub_f32_e32 v230, v203, v122
	v_pk_add_f32 v[88:89], v[88:89], v[230:231]
	v_pk_add_f32 v[120:121], v[120:121], 1.0 op_sel_hi:[1,0]
	v_cvt_pk_bf16_f32 v101, v122, v123
	v_log_f32_e32 v120, v120
	v_log_f32_e32 v121, v121
	s_nop 0
	v_pk_add_f32 v[120:121], v[120:121], v[124:125]
	v_exp_f32_e64 v124, -|v92|
	v_exp_f32_e64 v125, -|v93|
	v_sub_f32_e32 v233, v203, v121
	v_sub_f32_e32 v232, v203, v120
	v_pk_add_f32 v[90:91], v[90:91], v[232:233]
	v_pk_add_f32 v[124:125], v[124:125], 1.0 op_sel_hi:[1,0]
	s_nop 0
	v_log_f32_e32 v124, v124
	v_log_f32_e32 v125, v125
	s_nop 0
	v_pk_add_f32 v[124:125], v[124:125], v[126:127]
	v_exp_f32_e64 v126, -|v94|
	v_exp_f32_e64 v127, -|v95|
	v_sub_f32_e32 v235, v203, v125
	v_sub_f32_e32 v234, v203, v124
	v_pk_add_f32 v[92:93], v[92:93], v[234:235]
	v_pk_add_f32 v[126:127], v[126:127], 1.0 op_sel_hi:[1,0]
	s_nop 0
	v_log_f32_e32 v126, v126
	v_log_f32_e32 v127, v127
	s_nop 0
	v_pk_add_f32 v[126:127], v[126:127], v[128:129]
	v_exp_f32_e64 v128, -|v96|
	v_exp_f32_e64 v129, -|v97|
	v_sub_f32_e32 v237, v203, v127
	v_sub_f32_e32 v236, v203, v126
	v_pk_add_f32 v[94:95], v[94:95], v[236:237]
	v_pk_add_f32 v[128:129], v[128:129], 1.0 op_sel_hi:[1,0]
	s_nop 0
	v_log_f32_e32 v128, v128
	v_log_f32_e32 v129, v129
	s_nop 0
	v_pk_add_f32 v[128:129], v[128:129], v[208:209]
	s_nop 0
	v_sub_f32_e32 v239, v203, v129
	v_sub_f32_e32 v238, v203, v128
	v_pk_add_f32 v[96:97], v[96:97], v[238:239]
	v_pk_add_f32 v[208:209], v[114:115], v[116:117]
	s_nop 0
	v_mfma_f32_32x32x16_bf16 v[82:97], v[130:133], v[98:101], v[82:97]
	v_cvt_pk_bf16_f32 v98, v106, v107
	v_cvt_pk_bf16_f32 v99, v108, v109
	v_cvt_pk_bf16_f32 v100, v110, v111
	v_cvt_pk_bf16_f32 v101, v112, v113
	v_add_f32_e64 v208, v118, v208
	v_add_f32_e64 v209, v119, v209
	v_pk_add_f32 v[208:209], v[122:123], v[208:209]
	v_mfma_f32_32x32x16_bf16 v[66:81], v[134:137], v[98:101], v[66:81]
	v_cvt_pk_bf16_f32 v98, v120, v121
	v_cvt_pk_bf16_f32 v99, v124, v125
	v_cvt_pk_bf16_f32 v100, v126, v127
	v_cvt_pk_bf16_f32 v101, v128, v129
	v_add_f32_e64 v208, v120, v208
	v_add_f32_e64 v209, v121, v209
	s_nop 5
	v_exp_f32_e32 v66, v66
	v_mfma_f32_32x32x16_bf16 v[82:97], v[134:137], v[98:101], v[82:97]
	v_add_f32_e64 v208, v124, v208
	v_add_f32_e64 v209, v125, v209
	v_exp_f32_e32 v67, v67
	v_pk_add_f32 v[208:209], v[126:127], v[208:209]
	v_exp_f32_e32 v68, v68
	v_exp_f32_e32 v69, v69
	v_exp_f32_e32 v70, v70
	v_exp_f32_e32 v71, v71
	s_nop 3
	v_exp_f32_e32 v86, v86
	v_exp_f32_e32 v87, v87
	v_exp_f32_e32 v88, v88
	v_exp_f32_e32 v89, v89
	v_exp_f32_e32 v98, v82
	v_exp_f32_e32 v99, v83
	v_exp_f32_e32 v100, v84
	v_exp_f32_e32 v101, v85
	v_exp_f32_e32 v72, v72
	v_exp_f32_e32 v73, v73
	v_cvt_pk_bf16_f32 v226, v86, v87
	v_cvt_pk_bf16_f32 v227, v88, v89
	s_nop 0
	ds_read_b64_tr_b16 v[86:87], v244 offset:4096
	ds_read_b64_tr_b16 v[88:89], v244 offset:5120
	ds_read_b64_tr_b16 v[228:229], v244 offset:4608
	ds_read_b64_tr_b16 v[230:231], v244 offset:5632
	v_pk_add_f32 v[208:209], v[128:129], v[208:209]
	v_exp_f32_e32 v205, v90
	v_exp_f32_e32 v223, v91
	v_pk_add_f32 v[208:209], v[208:209], v[208:209] op_sel:[0,1] op_sel_hi:[1,0]
	v_exp_f32_e32 v232, v76
	v_mov_b32_e32 v207, v208
	s_nop 1
	v_permlane32_swap_b32_e32 v208, v207
	v_exp_f32_e32 v233, v92
	v_exp_f32_e32 v234, v77
	v_exp_f32_e32 v235, v93
	v_exp_f32_e32 v236, v78
	v_exp_f32_e32 v237, v94
	v_exp_f32_e32 v238, v79
	v_exp_f32_e32 v239, v95
	v_cvt_pk_bf16_f32 v82, v66, v67
	v_cvt_pk_bf16_f32 v83, v68, v69
	v_cvt_pk_bf16_f32 v84, v70, v71
	v_cvt_pk_bf16_f32 v85, v72, v73
	v_cvt_pk_bf16_f32 v224, v98, v99
	v_cvt_pk_bf16_f32 v225, v100, v101
	v_exp_f32_e32 v175, v74
	v_exp_f32_e32 v209, v75
	v_exp_f32_e32 v240, v80
	v_exp_f32_e32 v241, v96
	v_exp_f32_e32 v242, v81
	v_exp_f32_e32 v243, v97
	s_waitcnt lgkmcnt(2)
	v_mfma_f32_32x32x16_bf16 v[98:113], v[86:89], v[82:85], v[50:65]
	v_mfma_f32_32x32x16_bf16 v[66:81], v[86:89], v[224:227], v[18:33]
	s_waitcnt lgkmcnt(0)
	v_mfma_f32_32x32x16_bf16 v[114:129], v[228:231], v[82:85], v[34:49]
	v_mfma_f32_32x32x16_bf16 v[82:97], v[228:231], v[224:227], v[2:17]
	v_cvt_pk_bf16_f32 v228, v205, v223
	v_mov_b32_e32 v205, v208
	v_add_f32_e64 v204, v204, v206
	v_add_f32_e64 v205, v205, v207
	v_cvt_pk_bf16_f32 v225, v232, v234
	v_pk_add_f32 v[204:205], v[202:203], v[204:205] neg_lo:[0,1] neg_hi:[0,1]
	v_cvt_pk_bf16_f32 v226, v236, v238
	v_cvt_pk_bf16_f32 v229, v233, v235
	v_cvt_pk_bf16_f32 v230, v237, v239
	ds_read_b64_tr_b16 v[232:233], v244 offset:6144
	ds_read_b64_tr_b16 v[234:235], v244 offset:7168
	ds_read_b64_tr_b16 v[236:237], v244 offset:6656
	ds_read_b64_tr_b16 v[238:239], v244 offset:7680
	v_cmp_gt_f32_e32 vcc, s72, v204
	v_cmp_gt_f32_e64 s[0:1], s72, v205
	s_and_b64 s[0:1], vcc, s[0:1]
	v_cvt_pk_bf16_f32 v224, v175, v209
	v_cndmask_b32_e64 v175, 0, 1, s[0:1]
	v_cmp_ne_u32_e32 vcc, 0, v175
	v_cvt_pk_bf16_f32 v227, v240, v242
	v_cvt_pk_bf16_f32 v231, v241, v243
	s_cmp_lg_u64 vcc, exec
	s_waitcnt lgkmcnt(2)
	v_mfma_f32_32x32x16_bf16 v[98:113], v[232:235], v[224:227], v[98:113]
	s_cselect_b64 s[0:1], -1, 0
	v_mfma_f32_32x32x16_bf16 v[66:81], v[232:235], v[228:231], v[66:81]
	s_waitcnt lgkmcnt(0)
	v_mfma_f32_32x32x16_bf16 v[114:129], v[236:239], v[224:227], v[114:129]
	v_mfma_f32_32x32x16_bf16 v[82:97], v[236:239], v[228:231], v[82:97]
	s_branch .LBB0_271
.LBB0_270:
	ds_read_b128 v[82:85], v193
	s_waitcnt lgkmcnt(0)
	v_mfma_f32_32x32x16_bf16 v[66:81], v[170:173], v[142:145], 0
	s_mov_b64 s[0:1], -1
	v_mfma_f32_32x32x16_bf16 v[66:81], v[82:85], v[150:153], v[66:81]
	ds_read_b128 v[82:85], v191
	s_waitcnt lgkmcnt(0)
	v_mfma_f32_32x32x16_bf16 v[66:81], v[82:85], v[158:161], v[66:81]
	ds_read_b128 v[82:85], v189
	s_waitcnt lgkmcnt(0)
	v_mfma_f32_32x32x16_bf16 v[66:81], v[82:85], v[166:169], v[66:81]
	s_nop 11
	v_exp_f32_e64 v82, -|v66|
	v_exp_f32_e64 v83, -|v67|
	v_max_i32_e32 v85, 0, v67
	v_max_i32_e32 v84, 0, v66
	v_add_f32_e32 v82, 1.0, v82
	v_add_f32_e32 v83, 1.0, v83
	v_log_f32_e32 v82, v82
	v_log_f32_e32 v83, v83
	v_max_i32_e32 v87, 0, v69
	v_max_i32_e32 v86, 0, v68
	v_pk_add_f32 v[84:85], v[82:83], v[84:85]
	s_nop 0
	v_sub_f32_e32 v66, v66, v84
	v_cndmask_b32_e64 v92, v222, v66, s[4:5]
	v_cndmask_b32_e64 v83, 0, v85, s[2:3]
	v_cndmask_b32_e64 v82, 0, v84, s[4:5]
	v_sub_f32_e32 v66, v67, v85
	v_exp_f32_e64 v84, -|v68|
	v_exp_f32_e64 v85, -|v69|
	v_cndmask_b32_e64 v93, v222, v66, s[2:3]
	v_mov_b32_e32 v66, v83
	v_add_f32_e32 v84, 1.0, v84
	v_add_f32_e32 v85, 1.0, v85
	v_log_f32_e32 v84, v84
	v_log_f32_e32 v85, v85
	v_pk_add_f32 v[66:67], v[82:83], v[66:67]
	v_cvt_pk_bf16_f32 v82, v82, v83
	v_pk_add_f32 v[86:87], v[84:85], v[86:87]
	s_nop 0
	v_sub_f32_e32 v68, v68, v86
	v_cndmask_b32_e64 v94, v222, v68, s[8:9]
	v_cndmask_b32_e64 v85, 0, v87, s[6:7]
	v_cndmask_b32_e64 v84, 0, v86, s[8:9]
	v_sub_f32_e32 v68, v69, v87
	v_pk_add_f32 v[66:67], v[84:85], v[66:67]
	v_cndmask_b32_e64 v95, v222, v68, s[6:7]
	v_mov_b32_e32 v68, v85
	v_pk_add_f32 v[66:67], v[68:69], v[66:67]
	v_exp_f32_e64 v68, -|v70|
	v_exp_f32_e64 v69, -|v71|
	v_max_i32_e32 v87, 0, v71
	v_max_i32_e32 v86, 0, v70
	v_add_f32_e32 v68, 1.0, v68
	v_add_f32_e32 v69, 1.0, v69
	v_log_f32_e32 v68, v68
	v_log_f32_e32 v69, v69
	v_cvt_pk_bf16_f32 v83, v84, v85
	v_pk_add_f32 v[68:69], v[68:69], v[86:87]
	s_nop 0
	v_sub_f32_e32 v70, v70, v68
	v_cndmask_b32_e64 v87, 0, v69, s[10:11]
	v_cndmask_b32_e64 v86, 0, v68, s[12:13]
	v_sub_f32_e32 v68, v71, v69
	v_pk_add_f32 v[66:67], v[86:87], v[66:67]
	v_cndmask_b32_e64 v105, v222, v68, s[10:11]
	v_mov_b32_e32 v68, v87
	v_pk_add_f32 v[66:67], v[68:69], v[66:67]
	v_exp_f32_e64 v68, -|v72|
	v_exp_f32_e64 v69, -|v73|
	v_cndmask_b32_e64 v104, v222, v70, s[12:13]
	v_max_i32_e32 v71, 0, v73
	v_add_f32_e32 v68, 1.0, v68
	v_add_f32_e32 v69, 1.0, v69
	v_log_f32_e32 v68, v68
	v_log_f32_e32 v69, v69
	v_max_i32_e32 v70, 0, v72
	v_cvt_pk_bf16_f32 v84, v86, v87
	v_pk_add_f32 v[68:69], v[68:69], v[70:71]
	s_nop 0
	v_sub_f32_e32 v70, v72, v68
	v_cndmask_b32_e64 v89, 0, v69, s[14:15]
	v_cndmask_b32_e64 v88, 0, v68, s[16:17]
	v_sub_f32_e32 v68, v73, v69
	v_pk_add_f32 v[66:67], v[88:89], v[66:67]
	v_cndmask_b32_e64 v107, v222, v68, s[14:15]
	v_mov_b32_e32 v68, v89
	v_pk_add_f32 v[66:67], v[68:69], v[66:67]
	v_exp_f32_e64 v68, -|v74|
	v_exp_f32_e64 v69, -|v75|
	v_cndmask_b32_e64 v106, v222, v70, s[16:17]
	v_max_i32_e32 v71, 0, v75
	v_add_f32_e32 v68, 1.0, v68
	v_add_f32_e32 v69, 1.0, v69
	v_log_f32_e32 v68, v68
	v_log_f32_e32 v69, v69
	v_max_i32_e32 v70, 0, v74
	v_mov_b32_e32 v72, v203
	v_mov_b32_e32 v73, v203
	v_pk_add_f32 v[68:69], v[68:69], v[70:71]
	v_max_i32_e32 v71, 0, v77
	v_sub_f32_e32 v70, v74, v68
	v_cndmask_b32_e64 v91, 0, v69, s[18:19]
	v_cndmask_b32_e64 v90, 0, v68, s[20:21]
	v_sub_f32_e32 v68, v75, v69
	v_pk_add_f32 v[66:67], v[90:91], v[66:67]
	v_cndmask_b32_e64 v109, v222, v68, s[18:19]
	v_mov_b32_e32 v68, v91
	v_pk_add_f32 v[66:67], v[68:69], v[66:67]
	v_exp_f32_e64 v68, -|v76|
	v_exp_f32_e64 v69, -|v77|
	v_cndmask_b32_e64 v108, v222, v70, s[20:21]
	v_max_i32_e32 v70, 0, v76
	v_add_f32_e32 v68, 1.0, v68
	v_add_f32_e32 v69, 1.0, v69
	v_log_f32_e32 v68, v68
	v_log_f32_e32 v69, v69
	v_mov_b32_e32 v74, v203
	v_mov_b32_e32 v75, v203
	v_cvt_pk_bf16_f32 v85, v88, v89
	v_pk_add_f32 v[68:69], v[68:69], v[70:71]
	v_max_i32_e32 v71, 0, v79
	v_sub_f32_e32 v70, v76, v68
	v_cndmask_b32_e64 v97, 0, v69, s[22:23]
	v_cndmask_b32_e64 v96, 0, v68, s[24:25]
	v_sub_f32_e32 v68, v77, v69
	v_pk_add_f32 v[66:67], v[96:97], v[66:67]
	v_cndmask_b32_e64 v111, v222, v68, s[22:23]
	v_mov_b32_e32 v68, v97
	v_pk_add_f32 v[66:67], v[68:69], v[66:67]
	v_exp_f32_e64 v68, -|v78|
	v_exp_f32_e64 v69, -|v79|
	v_cndmask_b32_e64 v110, v222, v70, s[24:25]
	v_max_i32_e32 v70, 0, v78
	v_add_f32_e32 v68, 1.0, v68
	v_add_f32_e32 v69, 1.0, v69
	v_log_f32_e32 v68, v68
	v_log_f32_e32 v69, v69
	v_mov_b32_e32 v76, v203
	v_mov_b32_e32 v77, v203
	v_pk_add_f32 v[68:69], v[68:69], v[70:71]
	s_nop 0
	v_sub_f32_e32 v70, v78, v68
	v_cndmask_b32_e64 v99, 0, v69, s[26:27]
	v_cndmask_b32_e64 v98, 0, v68, s[28:29]
	v_sub_f32_e32 v68, v79, v69
	v_pk_add_f32 v[66:67], v[98:99], v[66:67]
	v_cndmask_b32_e64 v113, v222, v68, s[26:27]
	v_mov_b32_e32 v68, v99
	v_pk_add_f32 v[66:67], v[68:69], v[66:67]
	v_exp_f32_e64 v68, -|v80|
	v_exp_f32_e64 v69, -|v81|
	v_cndmask_b32_e64 v112, v222, v70, s[28:29]
	v_max_i32_e32 v71, 0, v81
	v_add_f32_e32 v68, 1.0, v68
	v_add_f32_e32 v69, 1.0, v69
	v_log_f32_e32 v68, v68
	v_log_f32_e32 v69, v69
	v_max_i32_e32 v70, 0, v80
	v_mov_b32_e32 v78, v203
	v_mov_b32_e32 v79, v203
	v_pk_add_f32 v[68:69], v[68:69], v[70:71]
	v_mov_b32_e32 v71, v203
	v_sub_f32_e32 v70, v80, v68
	v_cndmask_b32_e64 v101, 0, v69, s[30:31]
	v_cndmask_b32_e64 v100, 0, v68, s[34:35]
	v_sub_f32_e32 v68, v81, v69
	v_pk_add_f32 v[66:67], v[100:101], v[66:67]
	v_cndmask_b32_e64 v115, v222, v68, s[30:31]
	v_mov_b32_e32 v68, v101
	v_cndmask_b32_e64 v114, v222, v70, s[34:35]
	v_pk_add_f32 v[102:103], v[68:69], v[66:67]
	v_mov_b32_e32 v66, v203
	v_mov_b32_e32 v67, v203
	v_mov_b32_e32 v68, v203
	v_mov_b32_e32 v69, v203
	v_mov_b32_e32 v70, v203
	v_mov_b32_e32 v80, v203
	v_mov_b32_e32 v81, v203
	v_mov_b32_e32 v103, v102
	s_nop 1
	v_permlane32_swap_b32_e32 v102, v103
	v_mfma_f32_32x32x16_bf16 v[66:81], v[130:133], v[82:85], v[66:81]
	v_cvt_pk_bf16_f32 v82, v90, v91
	v_cvt_pk_bf16_f32 v83, v96, v97
	v_cvt_pk_bf16_f32 v84, v98, v99
	v_cvt_pk_bf16_f32 v85, v100, v101
	s_nop 1
	v_mfma_f32_32x32x16_bf16 v[66:81], v[134:137], v[82:85], v[66:81]
	v_add_f32_e32 v82, v102, v103
	v_sub_f32_e32 v203, v203, v82
	v_mov_b64_e32 v[204:205], v[202:203]
	s_nop 8
	v_add_f32_e32 v66, v66, v92
	v_add_f32_e32 v67, v67, v93
	v_add_f32_e32 v68, v68, v94
	v_add_f32_e32 v69, v69, v95
	v_add_f32_e32 v72, v72, v106
	v_add_f32_e32 v73, v73, v107
	v_add_f32_e32 v78, v78, v112
	v_add_f32_e32 v79, v79, v113
	v_exp_f32_e32 v66, v66
	v_exp_f32_e32 v67, v67
	v_exp_f32_e32 v68, v68
	v_exp_f32_e32 v69, v69
	v_add_f32_e32 v70, v70, v104
	v_add_f32_e32 v71, v71, v105
	v_exp_f32_e32 v72, v72
	v_exp_f32_e32 v73, v73
	v_add_f32_e32 v74, v74, v108
	v_add_f32_e32 v75, v75, v109
	v_add_f32_e32 v76, v76, v110
	v_add_f32_e32 v77, v77, v111
	v_exp_f32_e32 v78, v78
	v_exp_f32_e32 v79, v79
	v_exp_f32_e32 v70, v70
	v_exp_f32_e32 v71, v71
	v_exp_f32_e32 v74, v74
	v_exp_f32_e32 v75, v75
	v_exp_f32_e32 v76, v76
	v_exp_f32_e32 v77, v77
	v_cvt_pk_bf16_f32 v66, v66, v67
	v_cvt_pk_bf16_f32 v67, v68, v69
	v_cvt_pk_bf16_f32 v69, v72, v73
	v_cvt_pk_bf16_f32 v72, v78, v79
	v_add_u32_e32 v78, s81, v210
	v_cvt_pk_bf16_f32 v68, v70, v71
	v_cvt_pk_bf16_f32 v70, v74, v75
	v_cvt_pk_bf16_f32 v71, v76, v77
	s_nop 0
	ds_read_b64_tr_b16 v[74:75], v78 offset:4096
	ds_read_b64_tr_b16 v[76:77], v78 offset:5120
	s_waitcnt lgkmcnt(0)
	v_mfma_f32_32x32x16_bf16 v[18:33], v[74:77], v[66:69], v[18:33]
	ds_read_b64_tr_b16 v[74:75], v78 offset:4608
	ds_read_b64_tr_b16 v[76:77], v78 offset:5632
	v_add_f32_e32 v80, v80, v114
	v_add_f32_e32 v81, v81, v115
	v_exp_f32_e32 v80, v80
	v_exp_f32_e32 v81, v81
	v_mov_b64_e32 v[128:129], v[48:49]
	v_mov_b64_e32 v[112:113], v[64:65]
	s_waitcnt lgkmcnt(0)
	v_mfma_f32_32x32x16_bf16 v[2:17], v[74:77], v[66:69], v[2:17]
	ds_read_b64_tr_b16 v[66:67], v78 offset:6144
	ds_read_b64_tr_b16 v[68:69], v78 offset:7168
	v_cvt_pk_bf16_f32 v73, v80, v81
	v_mov_b64_e32 v[126:127], v[46:47]
	v_mov_b64_e32 v[124:125], v[44:45]
	v_mov_b64_e32 v[122:123], v[42:43]
	v_mov_b64_e32 v[120:121], v[40:41]
	v_mov_b64_e32 v[118:119], v[38:39]
	s_waitcnt lgkmcnt(0)
	v_mfma_f32_32x32x16_bf16 v[18:33], v[66:69], v[70:73], v[18:33]
	ds_read_b64_tr_b16 v[66:67], v78 offset:6656
	ds_read_b64_tr_b16 v[68:69], v78 offset:7680
	v_mov_b64_e32 v[116:117], v[36:37]
	v_mov_b64_e32 v[114:115], v[34:35]
	v_mov_b64_e32 v[110:111], v[62:63]
	v_mov_b64_e32 v[108:109], v[60:61]
	v_mov_b64_e32 v[106:107], v[58:59]
	v_mov_b64_e32 v[104:105], v[56:57]
	s_waitcnt lgkmcnt(0)
	v_mfma_f32_32x32x16_bf16 v[2:17], v[66:69], v[70:73], v[2:17]
	s_nop 1
	v_mov_b64_e32 v[80:81], v[32:33]
	v_mov_b64_e32 v[78:79], v[30:31]
	v_mov_b64_e32 v[76:77], v[28:29]
	v_mov_b64_e32 v[74:75], v[26:27]
	v_mov_b64_e32 v[72:73], v[24:25]
	v_mov_b64_e32 v[70:71], v[22:23]
	v_mov_b64_e32 v[68:69], v[20:21]
	s_nop 2
	v_mov_b64_e32 v[96:97], v[16:17]
	v_mov_b64_e32 v[94:95], v[14:15]
	v_mov_b64_e32 v[92:93], v[12:13]
	v_mov_b64_e32 v[90:91], v[10:11]
	v_mov_b64_e32 v[88:89], v[8:9]
	v_mov_b64_e32 v[86:87], v[6:7]
	v_mov_b64_e32 v[84:85], v[4:5]
	v_mov_b64_e32 v[82:83], v[2:3]
	v_mov_b64_e32 v[66:67], v[18:19]
	v_mov_b64_e32 v[102:103], v[54:55]
	v_mov_b64_e32 v[100:101], v[52:53]
	v_mov_b64_e32 v[98:99], v[50:51]

.LBB0_2751:
	ds_read_b64 v[226:227], v146
	v_add_u32_e32 v179, s39, v151
	v_add_u32_e32 v225, v179, v155
	v_add_u32_e32 v224, v179, v181
	v_add_u32_e32 v223, v179, v219
	s_waitcnt lgkmcnt(0)
	v_lshrrev_b32_e32 v82, v163, v226
	v_bfe_i32 v83, v82, 26, 1
	v_bitop3_b32 v96, v16, s28, v83 bitop3:0xe4
	v_bfe_i32 v83, v82, 25, 1
	v_bitop3_b32 v95, v13, s28, v83 bitop3:0xe4
	v_bfe_i32 v83, v82, 24, 1
	v_bitop3_b32 v94, v14, s28, v83 bitop3:0xe4
	v_bfe_i32 v83, v82, 19, 1
	v_bitop3_b32 v93, v11, s28, v83 bitop3:0xe4
	v_bfe_i32 v83, v82, 18, 1
	v_bitop3_b32 v92, v12, s28, v83 bitop3:0xe4
	v_bfe_i32 v83, v82, 17, 1
	v_add_u32_e32 v226, v179, v153
	v_bitop3_b32 v91, v9, s28, v83 bitop3:0xe4
	v_bfe_i32 v83, v82, 16, 1
	ds_read_b128 v[186:189], v226
	v_bitop3_b32 v90, v10, s28, v83 bitop3:0xe4
	v_bfe_i32 v83, v82, 11, 1
	v_bitop3_b32 v89, v7, s28, v83 bitop3:0xe4
	v_bfe_i32 v83, v82, 10, 1
	v_bitop3_b32 v88, v8, s28, v83 bitop3:0xe4
	v_bfe_i32 v83, v82, 9, 1
	v_bitop3_b32 v87, v5, s28, v83 bitop3:0xe4
	v_bfe_i32 v83, v82, 8, 1
	v_bitop3_b32 v86, v6, s28, v83 bitop3:0xe4
	v_bfe_i32 v83, v82, 3, 1
	v_bfe_i32 v84, v82, 27, 1
	v_bitop3_b32 v85, v3, s28, v83 bitop3:0xe4
	v_bfe_i32 v83, v82, 2, 1
	v_bitop3_b32 v97, v15, s28, v84 bitop3:0xe4
	v_bitop3_b32 v84, v4, s28, v83 bitop3:0xe4
	v_bfe_i32 v83, v82, 1, 1
	v_bfe_i32 v82, v82, 0, 1
	v_bitop3_b32 v83, v1, s28, v83 bitop3:0xe4
	v_bitop3_b32 v82, v2, s28, v82 bitop3:0xe4
	v_add_u32_e32 v179, s39, v17
	s_add_i32 s14, s37, 1
	s_waitcnt lgkmcnt(0)
	v_mfma_f32_32x32x16_bf16 v[98:113], v[186:189], v[114:117], v[82:97]
	s_cmp_lg_u32 s37, 2
	s_cselect_b32 s37, s14, 0
	s_add_u32 s0, s0, 0x4000
	s_addc_u32 s1, s1, 0
	s_add_i32 s38, s38, 1
	s_cmp_eq_u32 s36, s0
	v_add_u32_e32 v146, 8, v146
	v_mfma_f32_32x32x16_bf16 v[82:97], v[186:189], v[130:133], v[82:97]
	ds_read_b128 v[186:189], v225
	s_waitcnt lgkmcnt(0)
	v_mfma_f32_32x32x16_bf16 v[98:113], v[186:189], v[118:121], v[98:113]
	v_mfma_f32_32x32x16_bf16 v[82:97], v[186:189], v[134:137], v[82:97]
	ds_read_b128 v[186:189], v224
	s_waitcnt lgkmcnt(0)
	v_mfma_f32_32x32x16_bf16 v[98:113], v[186:189], v[122:125], v[98:113]
	v_mfma_f32_32x32x16_bf16 v[82:97], v[186:189], v[138:141], v[82:97]
	ds_read_b128 v[186:189], v223
	s_waitcnt lgkmcnt(0)
	v_mfma_f32_32x32x16_bf16 v[98:113], v[186:189], v[126:129], v[98:113]
	v_mfma_f32_32x32x16_bf16 v[82:97], v[186:189], v[142:145], v[82:97]
	s_nop 10
	v_exp_f32_e32 v190, v98
	v_exp_f32_e32 v191, v99
	v_exp_f32_e32 v192, v100
	v_exp_f32_e32 v193, v101
	s_nop 0
	ds_read_b64_tr_b16 v[98:99], v179 offset:49152
	ds_read_b64_tr_b16 v[100:101], v179 offset:50176
	v_exp_f32_e32 v188, v102
	v_exp_f32_e32 v189, v103
	v_exp_f32_e32 v186, v104
	v_exp_f32_e32 v187, v105
	ds_read_b64_tr_b16 v[212:213], v179 offset:50688
	ds_read_b64_tr_b16 v[210:211], v179 offset:49664
	v_exp_f32_e32 v204, v82
	v_exp_f32_e32 v205, v83
	v_exp_f32_e32 v208, v84
	v_exp_f32_e32 v209, v85
	v_exp_f32_e32 v200, v86
	v_exp_f32_e32 v201, v87
	v_exp_f32_e32 v196, v88
	v_exp_f32_e32 v197, v89
	v_cvt_pk_bf16_f32 v102, v190, v191
	v_cvt_pk_bf16_f32 v103, v192, v193
	v_cvt_pk_bf16_f32 v104, v188, v189
	v_cvt_pk_bf16_f32 v105, v186, v187
	v_cvt_pk_bf16_f32 v82, v204, v205
	v_cvt_pk_bf16_f32 v83, v208, v209
	s_waitcnt lgkmcnt(2)
	v_mfma_f32_32x32x16_bf16 v[66:81], v[98:101], v[102:105], v[66:81]
	v_cvt_pk_bf16_f32 v84, v200, v201
	v_cvt_pk_bf16_f32 v85, v196, v197
	v_exp_f32_e32 v206, v106
	v_exp_f32_e32 v207, v107
	v_exp_f32_e32 v202, v108
	v_exp_f32_e32 v203, v109
	v_exp_f32_e32 v198, v110
	s_waitcnt lgkmcnt(0)
	v_mfma_f32_32x32x16_bf16 v[50:65], v[210:213], v[102:105], v[50:65]
	v_exp_f32_e32 v199, v111
	v_exp_f32_e32 v194, v112
	v_exp_f32_e32 v195, v113
	v_exp_f32_e32 v216, v90
	v_exp_f32_e32 v217, v91
	v_exp_f32_e32 v214, v92
	v_exp_f32_e32 v215, v93
	v_mfma_f32_32x32x16_bf16 v[34:49], v[98:101], v[82:85], v[34:49]
	v_cvt_pk_bf16_f32 v86, v206, v207
	v_cvt_pk_bf16_f32 v87, v202, v203
	v_cvt_pk_bf16_f32 v88, v198, v199
	v_cvt_pk_bf16_f32 v89, v194, v195
	v_mfma_f32_32x32x16_bf16 v[18:33], v[210:213], v[82:85], v[18:33]
	ds_read_b64_tr_b16 v[82:83], v179 offset:51200
	ds_read_b64_tr_b16 v[84:85], v179 offset:52224
	ds_read_b64_tr_b16 v[100:101], v179 offset:52736
	ds_read_b64_tr_b16 v[98:99], v179 offset:51712
	v_exp_f32_e32 v212, v94
	v_exp_f32_e32 v213, v95
	v_exp_f32_e32 v210, v96
	v_exp_f32_e32 v211, v97
	s_waitcnt lgkmcnt(2)
	v_mfma_f32_32x32x16_bf16 v[66:81], v[82:85], v[86:89], v[66:81]
	s_waitcnt lgkmcnt(0)
	v_mfma_f32_32x32x16_bf16 v[50:65], v[98:101], v[86:89], v[50:65]
	v_cvt_pk_bf16_f32 v86, v216, v217
	v_cvt_pk_bf16_f32 v87, v214, v215
	v_cvt_pk_bf16_f32 v88, v212, v213
	v_cvt_pk_bf16_f32 v89, v210, v211
	s_nop 1
	v_mfma_f32_32x32x16_bf16 v[34:49], v[82:85], v[86:89], v[34:49]
	v_lshrrev_b32_e32 v82, v163, v227
	v_bfe_i32 v83, v82, 26, 1
	v_bitop3_b32 v96, v16, s28, v83 bitop3:0xe4
	v_bfe_i32 v83, v82, 25, 1
	v_bitop3_b32 v95, v13, s28, v83 bitop3:0xe4
	v_bfe_i32 v83, v82, 24, 1
	v_bitop3_b32 v94, v14, s28, v83 bitop3:0xe4
	v_bfe_i32 v83, v82, 19, 1
	v_bitop3_b32 v93, v11, s28, v83 bitop3:0xe4
	v_bfe_i32 v83, v82, 18, 1
	v_bitop3_b32 v92, v12, s28, v83 bitop3:0xe4
	v_bfe_i32 v83, v82, 17, 1
	v_bitop3_b32 v91, v9, s28, v83 bitop3:0xe4
	v_bfe_i32 v83, v82, 16, 1
	ds_read_b128 v[226:229], v226 offset:4096
	v_bitop3_b32 v90, v10, s28, v83 bitop3:0xe4
	v_bfe_i32 v83, v82, 11, 1
	v_mfma_f32_32x32x16_bf16 v[18:33], v[98:101], v[86:89], v[18:33]
	v_bitop3_b32 v89, v7, s28, v83 bitop3:0xe4
	v_bfe_i32 v83, v82, 10, 1
	v_bitop3_b32 v88, v8, s28, v83 bitop3:0xe4
	v_bfe_i32 v83, v82, 9, 1
	v_bitop3_b32 v87, v5, s28, v83 bitop3:0xe4
	v_bfe_i32 v83, v82, 8, 1
	v_bitop3_b32 v86, v6, s28, v83 bitop3:0xe4
	v_bfe_i32 v83, v82, 3, 1
	v_bfe_i32 v84, v82, 27, 1
	v_bitop3_b32 v85, v3, s28, v83 bitop3:0xe4
	v_bfe_i32 v83, v82, 2, 1
	v_bitop3_b32 v97, v15, s28, v84 bitop3:0xe4
	v_bitop3_b32 v84, v4, s28, v83 bitop3:0xe4
	v_bfe_i32 v83, v82, 1, 1
	v_bfe_i32 v82, v82, 0, 1
	v_bitop3_b32 v83, v1, s28, v83 bitop3:0xe4
	v_bitop3_b32 v82, v2, s28, v82 bitop3:0xe4
	s_waitcnt lgkmcnt(0)
	s_nop 0
	v_mfma_f32_32x32x16_bf16 v[98:113], v[226:229], v[114:117], v[82:97]
	v_mfma_f32_32x32x16_bf16 v[82:97], v[226:229], v[130:133], v[82:97]
	ds_read_b128 v[226:229], v225 offset:4096
	s_waitcnt lgkmcnt(0)
	v_mfma_f32_32x32x16_bf16 v[98:113], v[226:229], v[118:121], v[98:113]
	v_mfma_f32_32x32x16_bf16 v[82:97], v[226:229], v[134:137], v[82:97]
	ds_read_b128 v[224:227], v224 offset:4096
	s_waitcnt lgkmcnt(0)
	v_mfma_f32_32x32x16_bf16 v[98:113], v[224:227], v[122:125], v[98:113]
	v_mfma_f32_32x32x16_bf16 v[82:97], v[224:227], v[138:141], v[82:97]
	ds_read_b128 v[224:227], v223 offset:4096
	s_waitcnt lgkmcnt(0)
	v_mfma_f32_32x32x16_bf16 v[98:113], v[224:227], v[126:129], v[98:113]
	v_mfma_f32_32x32x16_bf16 v[82:97], v[224:227], v[142:145], v[82:97]
	s_nop 10
	v_exp_f32_e32 v228, v98
	v_exp_f32_e32 v229, v99
	v_exp_f32_e32 v230, v100
	v_exp_f32_e32 v231, v101
	ds_read_b64_tr_b16 v[98:99], v179 offset:53248
	ds_read_b64_tr_b16 v[100:101], v179 offset:54272
	v_exp_f32_e32 v232, v102
	v_exp_f32_e32 v233, v103
	v_exp_f32_e32 v234, v104
	v_exp_f32_e32 v235, v105
	ds_read_b64_tr_b16 v[226:227], v179 offset:54784
	ds_read_b64_tr_b16 v[224:225], v179 offset:53760
	v_cvt_pk_bf16_f32 v102, v228, v229
	v_cvt_pk_bf16_f32 v103, v230, v231
	v_cvt_pk_bf16_f32 v104, v232, v233
	v_cvt_pk_bf16_f32 v105, v234, v235
	v_exp_f32_e32 v236, v86
	v_exp_f32_e32 v237, v87
	s_waitcnt lgkmcnt(2)
	v_mfma_f32_32x32x16_bf16 v[66:81], v[98:101], v[102:105], v[66:81]
	v_exp_f32_e32 v238, v88
	v_exp_f32_e32 v239, v89
	v_exp_f32_e32 v106, v106
	v_exp_f32_e32 v107, v107
	v_exp_f32_e32 v108, v108
	v_exp_f32_e32 v109, v109
	v_exp_f32_e32 v110, v110
	s_waitcnt lgkmcnt(0)
	v_mfma_f32_32x32x16_bf16 v[50:65], v[224:227], v[102:105], v[50:65]
	v_exp_f32_e32 v102, v82
	v_exp_f32_e32 v103, v83
	v_exp_f32_e32 v104, v84
	v_exp_f32_e32 v105, v85
	v_cvt_pk_bf16_f32 v84, v236, v237
	v_cvt_pk_bf16_f32 v82, v102, v103
	v_cvt_pk_bf16_f32 v85, v238, v239
	v_cvt_pk_bf16_f32 v83, v104, v105
	v_exp_f32_e32 v111, v111
	v_exp_f32_e32 v112, v112
	v_mfma_f32_32x32x16_bf16 v[34:49], v[98:101], v[82:85], v[34:49]
	v_exp_f32_e32 v113, v113
	v_exp_f32_e32 v90, v90
	v_exp_f32_e32 v91, v91
	v_exp_f32_e32 v92, v92
	v_exp_f32_e32 v93, v93
	v_exp_f32_e32 v94, v94
	v_exp_f32_e32 v95, v95
	v_mfma_f32_32x32x16_bf16 v[18:33], v[224:227], v[82:85], v[18:33]
	ds_read_b64_tr_b16 v[82:83], v179 offset:55296
	ds_read_b64_tr_b16 v[84:85], v179 offset:56320
	ds_read_b64_tr_b16 v[100:101], v179 offset:56832
	ds_read_b64_tr_b16 v[98:99], v179 offset:55808
	v_exp_f32_e32 v96, v96
	v_exp_f32_e32 v97, v97
	v_cvt_pk_bf16_f32 v86, v106, v107
	v_cvt_pk_bf16_f32 v87, v108, v109
	v_cvt_pk_bf16_f32 v88, v110, v111
	v_cvt_pk_bf16_f32 v89, v112, v113
	s_waitcnt lgkmcnt(2)
	s_nop 0
	v_mfma_f32_32x32x16_bf16 v[66:81], v[82:85], v[86:89], v[66:81]
	s_waitcnt lgkmcnt(0)
	v_mfma_f32_32x32x16_bf16 v[50:65], v[98:101], v[86:89], v[50:65]
	v_cvt_pk_bf16_f32 v86, v90, v91
	v_cvt_pk_bf16_f32 v87, v92, v93
	v_cvt_pk_bf16_f32 v88, v94, v95
	v_cvt_pk_bf16_f32 v89, v96, v97
	s_nop 1
	v_mfma_f32_32x32x16_bf16 v[34:49], v[82:85], v[86:89], v[34:49]
	v_add_f32_e64 v82, v190, 0
	v_add_f32_e64 v83, v191, 0
	v_add_f32_e64 v84, v228, 0
	v_add_f32_e64 v85, v229, 0
	v_add_f32_e64 v82, v192, v82
	v_add_f32_e64 v83, v193, v83
	v_pk_add_f32 v[84:85], v[230:231], v[84:85]
	v_pk_add_f32 v[82:83], v[188:189], v[82:83]
	v_pk_add_f32 v[84:85], v[232:233], v[84:85]
	v_pk_add_f32 v[82:83], v[186:187], v[82:83]
	v_mfma_f32_32x32x16_bf16 v[18:33], v[98:101], v[86:89], v[18:33]
	v_add_f32_e64 v86, v204, 0
	v_add_f32_e64 v87, v205, 0
	v_add_f32_e64 v88, v102, 0
	v_add_f32_e64 v89, v103, 0
	v_add_f32_e64 v86, v208, v86
	v_add_f32_e64 v87, v209, v87
	v_pk_add_f32 v[88:89], v[104:105], v[88:89]
	v_pk_add_f32 v[86:87], v[200:201], v[86:87]
	v_pk_add_f32 v[88:89], v[236:237], v[88:89]
	v_pk_add_f32 v[84:85], v[234:235], v[84:85]
	v_pk_add_f32 v[86:87], v[196:197], v[86:87]
	v_pk_add_f32 v[88:89], v[238:239], v[88:89]
	v_pk_add_f32 v[82:83], v[206:207], v[82:83]
	v_pk_add_f32 v[84:85], v[106:107], v[84:85]
	v_pk_add_f32 v[86:87], v[216:217], v[86:87]
	v_pk_add_f32 v[88:89], v[90:91], v[88:89]
	v_pk_add_f32 v[82:83], v[202:203], v[82:83]
	v_pk_add_f32 v[84:85], v[108:109], v[84:85]
	v_pk_add_f32 v[86:87], v[214:215], v[86:87]
	v_pk_add_f32 v[88:89], v[92:93], v[88:89]
	v_pk_add_f32 v[82:83], v[198:199], v[82:83]
	v_pk_add_f32 v[84:85], v[110:111], v[84:85]
	v_pk_add_f32 v[86:87], v[212:213], v[86:87]
	v_pk_add_f32 v[88:89], v[94:95], v[88:89]
	v_pk_add_f32 v[82:83], v[194:195], v[82:83]
	v_pk_add_f32 v[84:85], v[112:113], v[84:85]
	v_pk_add_f32 v[86:87], v[210:211], v[86:87]
	v_pk_add_f32 v[88:89], v[96:97], v[88:89]
	v_pk_add_f32 v[82:83], v[82:83], v[84:85]
	v_pk_add_f32 v[84:85], v[86:87], v[88:89]
	v_mov_b32_e32 v86, v82
	v_mov_b32_e32 v87, v84
	v_mov_b32_e32 v84, v83
	v_pk_add_f32 v[82:83], v[86:87], v[84:85]
	s_nop 0
	v_pk_add_f32 v[184:185], v[184:185], v[82:83]
	s_cbranch_scc1 .LBB0_2745
